# baseline (speedup 1.0000x reference)
.LBB1_9:
	s_or_b64 exec, exec, s[6:7]
	v_lshlrev_b32_e32 v3, 12, v0
	v_and_b32_e32 v6, 0x3f8000, v3
	v_mov_b32_e32 v7, 0
	v_lshrrev_b32_e32 v1, 3, v0
	v_lshl_add_u64 v[4:5], s[4:5], 0, v[6:7]
	v_and_b32_e32 v2, 7, v0
	v_mov_b32_e32 v3, v7
	v_lshlrev_b32_e32 v8, 2, v1
	v_add_u32_e32 v8, 0x1000, v8
	v_add_u32_e32 v9, 0x200, v8
	ds_read2_b32 v[16:17], v8 offset1:196
	ds_read2_b32 v[18:19], v9 offset1:196
	v_mov_b32_e32 v14, 1
	v_mov_b32_e32 v15, 2
	s_movk_i32 s3, 0x44
	s_mov_b64 s[14:15], 0x400000
	s_mov_b64 s[22:23], 0x80
	v_cmp_gt_u32_e64 s[24:25], s3, v1
	s_waitcnt lgkmcnt(0)
	v_add_u32_e32 v20, v16, v2
	v_add_u32_e32 v21, v18, v2
	v_cndmask_b32_e64 v19, v18, v19, s[24:25]
	v_lshlrev_b32_e32 v22, 4, v20
	v_mov_b32_e32 v23, 0
	v_lshlrev_b32_e32 v24, 4, v21
	v_mov_b32_e32 v25, 0
	v_lshl_add_u64 v[22:23], v[4:5], 0, v[22:23]
	v_lshl_add_u64 v[24:25], v[4:5], 0, v[24:25]
	v_lshl_add_u64 v[24:25], v[24:25], 0, s[14:15]
	v_add_u32_e32 v26, 8, v20
	v_add_u32_e32 v27, 8, v21
	v_cmp_lt_i32_e64 s[4:5], v20, v17
	v_cmp_lt_i32_e64 s[6:7], v26, v17
	v_cmp_lt_i32_e64 s[12:13], v21, v19
	v_cmp_lt_i32_e64 s[16:17], v27, v19
	v_add_u32_e32 v26, 8, v26
	v_add_u32_e32 v27, 8, v27
	v_cmp_lt_i32_e64 s[18:19], v26, v17
	v_cmp_lt_i32_e64 s[20:21], v27, v19
	s_mov_b64 exec, s[4:5]
	s_cbranch_execz .Lkb_p1_ld0
	global_load_dword v28, v[22:23], off
.Lkb_p1_ld0:
	s_mov_b64 exec, s[6:7]
	s_cbranch_execz .Lkb_p1_ld1
	global_load_dword v29, v[22:23], off offset:128
.Lkb_p1_ld1:
	s_mov_b64 exec, s[12:13]
	s_cbranch_execz .Lkb_p1_ld2
	global_load_dword v30, v[24:25], off
.Lkb_p1_ld2:
	s_mov_b64 exec, s[16:17]
	s_cbranch_execz .Lkb_p1_ld3
	global_load_dword v31, v[24:25], off offset:128
.Lkb_p1_ld3:
	s_waitcnt vmcnt(0)
	v_lshlrev_b32_sdwa v31, v15, v31 dst_sel:DWORD dst_unused:UNUSED_PAD src0_sel:DWORD src1_sel:WORD_1
	ds_add_u32 v31, v14 offset:6176
	s_mov_b64 exec, s[12:13]
	v_lshlrev_b32_sdwa v30, v15, v30 dst_sel:DWORD dst_unused:UNUSED_PAD src0_sel:DWORD src1_sel:WORD_1
	ds_add_u32 v30, v14 offset:6176
	s_mov_b64 exec, s[6:7]
	v_lshlrev_b32_sdwa v29, v15, v29 dst_sel:DWORD dst_unused:UNUSED_PAD src0_sel:DWORD src1_sel:WORD_1
	ds_add_u32 v29, v14 offset:6176
	s_mov_b64 exec, s[4:5]
	v_lshlrev_b32_sdwa v28, v15, v28 dst_sel:DWORD dst_unused:UNUSED_PAD src0_sel:DWORD src1_sel:WORD_1
	ds_add_u32 v28, v14 offset:6176
	s_mov_b64 exec, s[18:19]
	s_cbranch_execz .Lkb_p1_a_end
	v_lshl_add_u64 v[32:33], v[22:23], 0, s[22:23]
	v_lshl_add_u64 v[32:33], v[32:33], 0, s[22:23]
	s_mov_b64 s[4:5], 0
.Lkb_p1_a_loop:
	global_load_dword v28, v[32:33], off
	v_add_u32_e32 v26, 8, v26
	v_cmp_ge_i32_e64 s[6:7], v26, v17
	s_or_b64 s[4:5], s[6:7], s[4:5]
	v_lshl_add_u64 v[32:33], v[32:33], 0, s[22:23]
	s_waitcnt vmcnt(0)
	v_lshlrev_b32_sdwa v28, v15, v28 dst_sel:DWORD dst_unused:UNUSED_PAD src0_sel:DWORD src1_sel:WORD_1
	ds_add_u32 v28, v14 offset:6176
	s_andn2_b64 exec, exec, s[4:5]
	s_cbranch_execnz .Lkb_p1_a_loop
.Lkb_p1_a_end:
	s_mov_b64 exec, s[20:21]
	s_cbranch_execz .Lkb_p1_b_end
	v_lshl_add_u64 v[34:35], v[24:25], 0, s[22:23]
	v_lshl_add_u64 v[34:35], v[34:35], 0, s[22:23]
	s_mov_b64 s[4:5], 0
.Lkb_p1_b_loop:
	global_load_dword v28, v[34:35], off
	v_add_u32_e32 v27, 8, v27
	v_cmp_ge_i32_e64 s[6:7], v27, v19
	s_or_b64 s[4:5], s[6:7], s[4:5]
	v_lshl_add_u64 v[34:35], v[34:35], 0, s[22:23]
	s_waitcnt vmcnt(0)
	v_lshlrev_b32_sdwa v28, v15, v28 dst_sel:DWORD dst_unused:UNUSED_PAD src0_sel:DWORD src1_sel:WORD_1
	ds_add_u32 v28, v14 offset:6176
	s_andn2_b64 exec, exec, s[4:5]
	s_cbranch_execnz .Lkb_p1_b_loop
.Lkb_p1_b_end:
.LBB1_14:
	s_mov_b64 exec, -1
	v_cmp_gt_u32_e64 s[4:5], 64, v0
	s_waitcnt lgkmcnt(0)
	s_barrier
	s_and_saveexec_b64 s[6:7], s[4:5]
	s_cbranch_execz .LBB1_16
	v_lshlrev_b32_e32 v10, 3, v0
	ds_read_b64 v[6:7], v10 offset:6176
	v_add_u32_e32 v8, -1, v12
	v_cmp_lt_i32_e64 s[4:5], v8, v13
	v_add_u32_e32 v9, -2, v12
	v_add_u32_e32 v11, -4, v12
	v_cndmask_b32_e64 v8, v8, v12, s[4:5]
	v_lshlrev_b32_e32 v8, 2, v8
	s_waitcnt lgkmcnt(0)
	v_add_u32_e32 v7, v7, v6
	ds_bpermute_b32 v8, v8, v7
	v_cmp_lt_i32_e64 s[4:5], v9, v13
	s_waitcnt lgkmcnt(0)
	v_cndmask_b32_e64 v8, v8, 0, vcc
	v_cndmask_b32_e64 v9, v9, v12, s[4:5]
	v_lshlrev_b32_e32 v9, 2, v9
	v_add_u32_e32 v8, v8, v7
	ds_bpermute_b32 v9, v9, v8
	v_cmp_lt_i32_e32 vcc, v11, v13
	s_nop 1
	v_cndmask_b32_e32 v11, v11, v12, vcc
	v_cmp_lt_u32_e32 vcc, 1, v0
	s_waitcnt lgkmcnt(0)
	s_nop 0
	v_cndmask_b32_e32 v9, 0, v9, vcc
	v_add_u32_e32 v8, v9, v8
	v_lshlrev_b32_e32 v9, 2, v11
	ds_bpermute_b32 v9, v9, v8
	v_add_u32_e32 v11, -8, v12
	v_cmp_lt_u32_e32 vcc, 3, v0
	s_waitcnt lgkmcnt(0)
	s_nop 0
	v_cndmask_b32_e32 v9, 0, v9, vcc
	v_cmp_lt_i32_e32 vcc, v11, v13
	v_add_u32_e32 v8, v9, v8
	s_nop 0
	v_cndmask_b32_e32 v9, v11, v12, vcc
	v_lshlrev_b32_e32 v9, 2, v9
	ds_bpermute_b32 v9, v9, v8
	v_add_u32_e32 v11, -16, v12
	v_cmp_lt_u32_e32 vcc, 7, v0
	s_waitcnt lgkmcnt(0)
	s_nop 0
	v_cndmask_b32_e32 v9, 0, v9, vcc
	v_cmp_lt_i32_e32 vcc, v11, v13
	v_add_u32_e32 v8, v9, v8
	s_nop 0
	v_cndmask_b32_e32 v9, v11, v12, vcc
	v_lshlrev_b32_e32 v9, 2, v9
	ds_bpermute_b32 v9, v9, v8
	v_cmp_lt_u32_e32 vcc, 15, v0
	s_waitcnt lgkmcnt(0)
	s_nop 0
	v_cndmask_b32_e32 v9, 0, v9, vcc
	v_add_u32_e32 v8, v9, v8
	v_subrev_u32_e32 v9, 32, v12
	v_cmp_lt_i32_e32 vcc, v9, v13
	s_nop 1
	v_cndmask_b32_e32 v9, v9, v12, vcc
	v_lshlrev_b32_e32 v9, 2, v9
	ds_bpermute_b32 v9, v9, v8
	v_cmp_lt_u32_e32 vcc, 31, v0
	s_waitcnt lgkmcnt(0)
	s_nop 0
	v_cndmask_b32_e32 v9, 0, v9, vcc
	v_add_u32_e32 v8, v9, v8
	v_sub_u32_e32 v8, v8, v7
	v_add_u32_e32 v9, v8, v6
	ds_write_b64 v10, v[8:9] offset:6688

.LBB1_21:
	s_or_b64 exec, exec, s[4:5]
	v_lshlrev_b32_e32 v8, 2, v1
	v_add_u32_e32 v8, 0x1000, v8
	v_add_u32_e32 v9, 0x200, v8
	ds_read2_b32 v[16:17], v8 offset1:196
	ds_read2_b32 v[18:19], v9 offset1:196
	v_mov_b32_e32 v11, 1
	v_mov_b32_e32 v12, 2
	s_movk_i32 s3, 0x44
	s_mov_b64 s[14:15], 0x400000
	s_mov_b64 s[22:23], 0x80
	v_cmp_gt_u32_e64 s[24:25], s3, v1
	s_waitcnt lgkmcnt(0)
	v_add_u32_e32 v20, v16, v2
	v_add_u32_e32 v21, v18, v2
	v_cndmask_b32_e64 v19, v18, v19, s[24:25]
	v_lshlrev_b32_e32 v22, 4, v20
	v_mov_b32_e32 v23, 0
	v_lshlrev_b32_e32 v24, 4, v21
	v_mov_b32_e32 v25, 0
	v_lshl_add_u64 v[22:23], v[4:5], 0, v[22:23]
	v_lshl_add_u64 v[24:25], v[4:5], 0, v[24:25]
	v_lshl_add_u64 v[24:25], v[24:25], 0, s[14:15]
	v_add_u32_e32 v26, 8, v20
	v_add_u32_e32 v27, 8, v21
	v_cmp_lt_i32_e64 s[4:5], v20, v17
	v_cmp_lt_i32_e64 s[6:7], v26, v17
	v_cmp_lt_i32_e64 s[12:13], v21, v19
	v_cmp_lt_i32_e64 s[16:17], v27, v19
	v_add_u32_e32 v26, 8, v26
	v_add_u32_e32 v27, 8, v27
	v_cmp_lt_i32_e64 s[18:19], v26, v17
	v_cmp_lt_i32_e64 s[20:21], v27, v19
	s_mov_b64 exec, s[4:5]
	s_cbranch_execz .Lkb_p2_ld0
	global_load_dwordx4 v[36:39], v[22:23], off
.Lkb_p2_ld0:
	s_mov_b64 exec, s[6:7]
	s_cbranch_execz .Lkb_p2_ld1
	global_load_dwordx4 v[40:43], v[22:23], off offset:128
.Lkb_p2_ld1:
	s_mov_b64 exec, s[12:13]
	s_cbranch_execz .Lkb_p2_ld2
	global_load_dwordx4 v[44:47], v[24:25], off
.Lkb_p2_ld2:
	s_mov_b64 exec, s[16:17]
	s_cbranch_execz .Lkb_p2_ld3
	global_load_dwordx4 v[48:51], v[24:25], off offset:128
.Lkb_p2_ld3:
	s_waitcnt vmcnt(0)
	v_lshlrev_b32_sdwa v31, v12, v48 dst_sel:DWORD dst_unused:UNUSED_PAD src0_sel:DWORD src1_sel:WORD_1
	ds_add_rtn_u32 v58, v31, v11 offset:5664
	ds_read_b32 v31, v31 offset:6688
	v_and_b32_e32 v48, 0xffff, v48
	s_mov_b64 exec, s[12:13]
	v_lshlrev_b32_sdwa v30, v12, v44 dst_sel:DWORD dst_unused:UNUSED_PAD src0_sel:DWORD src1_sel:WORD_1
	ds_add_rtn_u32 v56, v30, v11 offset:5664
	ds_read_b32 v30, v30 offset:6688
	v_and_b32_e32 v44, 0xffff, v44
	s_mov_b64 exec, s[6:7]
	v_lshlrev_b32_sdwa v29, v12, v40 dst_sel:DWORD dst_unused:UNUSED_PAD src0_sel:DWORD src1_sel:WORD_1
	ds_add_rtn_u32 v54, v29, v11 offset:5664
	ds_read_b32 v29, v29 offset:6688
	v_and_b32_e32 v40, 0xffff, v40
	s_mov_b64 exec, s[4:5]
	v_lshlrev_b32_sdwa v28, v12, v36 dst_sel:DWORD dst_unused:UNUSED_PAD src0_sel:DWORD src1_sel:WORD_1
	ds_add_rtn_u32 v52, v28, v11 offset:5664
	ds_read_b32 v28, v28 offset:6688
	v_and_b32_e32 v36, 0xffff, v36
	s_waitcnt lgkmcnt(0)
	v_add3_u32 v52, v52, v10, v28
	v_ashrrev_i32_e32 v53, 31, v52
	v_lshl_add_u64 v[52:53], v[52:53], 4, s[10:11]
	s_cbranch_execz .Lkb_p2_st0
	global_store_dwordx4 v[52:53], v[36:39], off
.Lkb_p2_st0:
	s_mov_b64 exec, s[6:7]
	v_add3_u32 v54, v54, v10, v29
	v_ashrrev_i32_e32 v55, 31, v54
	v_lshl_add_u64 v[54:55], v[54:55], 4, s[10:11]
	s_cbranch_execz .Lkb_p2_st1
	global_store_dwordx4 v[54:55], v[40:43], off
.Lkb_p2_st1:
	s_mov_b64 exec, s[12:13]
	v_add3_u32 v56, v56, v10, v30
	v_ashrrev_i32_e32 v57, 31, v56
	v_lshl_add_u64 v[56:57], v[56:57], 4, s[10:11]
	s_cbranch_execz .Lkb_p2_st2
	global_store_dwordx4 v[56:57], v[44:47], off
.Lkb_p2_st2:
	s_mov_b64 exec, s[16:17]
	v_add3_u32 v58, v58, v10, v31
	v_ashrrev_i32_e32 v59, 31, v58
	v_lshl_add_u64 v[58:59], v[58:59], 4, s[10:11]
	s_cbranch_execz .Lkb_p2_st3
	global_store_dwordx4 v[58:59], v[48:51], off
.Lkb_p2_st3:
	s_mov_b64 exec, s[18:19]
	s_cbranch_execz .Lkb_p2_a_end
	v_lshl_add_u64 v[32:33], v[22:23], 0, s[22:23]
	v_lshl_add_u64 v[32:33], v[32:33], 0, s[22:23]
	s_mov_b64 s[4:5], 0
.Lkb_p2_a_loop:
	global_load_dwordx4 v[36:39], v[32:33], off
	v_add_u32_e32 v26, 8, v26
	v_cmp_ge_i32_e64 s[6:7], v26, v17
	s_or_b64 s[4:5], s[6:7], s[4:5]
	v_lshl_add_u64 v[32:33], v[32:33], 0, s[22:23]
	s_waitcnt vmcnt(0)
	v_lshlrev_b32_sdwa v28, v12, v36 dst_sel:DWORD dst_unused:UNUSED_PAD src0_sel:DWORD src1_sel:WORD_1
	ds_add_rtn_u32 v52, v28, v11 offset:5664
	ds_read_b32 v28, v28 offset:6688
	v_and_b32_e32 v36, 0xffff, v36
	s_waitcnt lgkmcnt(0)
	v_add3_u32 v52, v52, v10, v28
	v_ashrrev_i32_e32 v53, 31, v52
	v_lshl_add_u64 v[52:53], v[52:53], 4, s[10:11]
	global_store_dwordx4 v[52:53], v[36:39], off
	s_andn2_b64 exec, exec, s[4:5]
	s_cbranch_execnz .Lkb_p2_a_loop

.Lkb_p2_b_loop:
	global_load_dwordx4 v[36:39], v[34:35], off
	v_add_u32_e32 v27, 8, v27
	v_cmp_ge_i32_e64 s[6:7], v27, v19
	s_or_b64 s[4:5], s[6:7], s[4:5]
	v_lshl_add_u64 v[34:35], v[34:35], 0, s[22:23]
	s_waitcnt vmcnt(0)
	v_lshlrev_b32_sdwa v28, v12, v36 dst_sel:DWORD dst_unused:UNUSED_PAD src0_sel:DWORD src1_sel:WORD_1
	ds_add_rtn_u32 v52, v28, v11 offset:5664
	ds_read_b32 v28, v28 offset:6688
	v_and_b32_e32 v36, 0xffff, v36
	s_waitcnt lgkmcnt(0)
	v_add3_u32 v52, v52, v10, v28
	v_ashrrev_i32_e32 v53, 31, v52
	v_lshl_add_u64 v[52:53], v[52:53], 4, s[10:11]
	global_store_dwordx4 v[52:53], v[36:39], off
	s_andn2_b64 exec, exec, s[4:5]
	s_cbranch_execnz .Lkb_p2_b_loop
.Lkb_p2_b_end:
.LBB1_26:
	s_mov_b64 exec, -1
	s_mov_b64 s[4:5], 0

.LBB1_32:
	s_endpgm
	s_nop 0
	s_nop 0
	s_nop 0
	s_endpgm

	.amdhsa_kernel _ZN12_GLOBAL__N_18k_bucketEPK15HIP_vector_typeIjLj4EEPKiPiPS1_PKfS9_PDF16_PfSB_
		.amdhsa_group_segment_fixed_size 7268
		.amdhsa_private_segment_fixed_size 0
		.amdhsa_kernarg_size 72
		.amdhsa_user_sgpr_count 2
		.amdhsa_user_sgpr_dispatch_ptr 0
		.amdhsa_user_sgpr_queue_ptr 0
		.amdhsa_user_sgpr_kernarg_segment_ptr 1
		.amdhsa_user_sgpr_dispatch_id 0
		.amdhsa_user_sgpr_kernarg_preload_length 0
		.amdhsa_user_sgpr_kernarg_preload_offset 0
		.amdhsa_user_sgpr_private_segment_size 0
		.amdhsa_uses_dynamic_stack 0
		.amdhsa_enable_private_segment 0
		.amdhsa_system_sgpr_workgroup_id_x 1
		.amdhsa_system_sgpr_workgroup_id_y 0
		.amdhsa_system_sgpr_workgroup_id_z 0
		.amdhsa_system_sgpr_workgroup_info 0
		.amdhsa_system_vgpr_workitem_id 0
		.amdhsa_next_free_vgpr 62
		.amdhsa_next_free_sgpr 26
		.amdhsa_accum_offset 64
		.amdhsa_reserve_vcc 1
		.amdhsa_float_round_mode_32 0
		.amdhsa_float_round_mode_16_64 0
		.amdhsa_float_denorm_mode_32 3
		.amdhsa_float_denorm_mode_16_64 3
		.amdhsa_dx10_clamp 1
		.amdhsa_ieee_mode 1
		.amdhsa_fp16_overflow 0
		.amdhsa_tg_split 0
		.amdhsa_exception_fp_ieee_invalid_op 0
		.amdhsa_exception_fp_denorm_src 0
		.amdhsa_exception_fp_ieee_div_zero 0
		.amdhsa_exception_fp_ieee_overflow 0
		.amdhsa_exception_fp_ieee_underflow 0
		.amdhsa_exception_fp_ieee_inexact 0
		.amdhsa_exception_int_div_zero 0
	.end_amdhsa_kernel

amdhsa.kernels:
  - .agpr_count:     0
    .args:
      - .actual_access:  read_only
        .address_space:  global
        .offset:         0
        .size:           8
        .value_kind:     global_buffer
      - .actual_access:  read_only
        .address_space:  global
        .offset:         8
        .size:           8
        .value_kind:     global_buffer
      - .actual_access:  read_only
        .address_space:  global
        .offset:         16
        .size:           8
        .value_kind:     global_buffer
      - .actual_access:  read_only
        .address_space:  global
        .offset:         24
        .size:           8
        .value_kind:     global_buffer
      - .actual_access:  read_only
        .address_space:  global
        .offset:         32
        .size:           8
        .value_kind:     global_buffer
      - .actual_access:  read_only
        .address_space:  global
        .offset:         40
        .size:           8
        .value_kind:     global_buffer
      - .actual_access:  read_only
        .address_space:  global
        .offset:         48
        .size:           8
        .value_kind:     global_buffer
      - .actual_access:  read_only
        .address_space:  global
        .offset:         56
        .size:           8
        .value_kind:     global_buffer
      - .actual_access:  read_only
        .address_space:  global
        .offset:         64
        .size:           8
        .value_kind:     global_buffer
      - .actual_access:  read_only
        .address_space:  global
        .offset:         72
        .size:           8
        .value_kind:     global_buffer
      - .actual_access:  read_only
        .address_space:  global
        .offset:         80
        .size:           8
        .value_kind:     global_buffer
      - .actual_access:  read_only
        .address_space:  global
        .offset:         88
        .size:           8
        .value_kind:     global_buffer
      - .actual_access:  write_only
        .address_space:  global
        .offset:         96
        .size:           8
        .value_kind:     global_buffer
      - .actual_access:  write_only
        .address_space:  global
        .offset:         104
        .size:           8
        .value_kind:     global_buffer
      - .actual_access:  write_only
        .address_space:  global
        .offset:         112
        .size:           8
        .value_kind:     global_buffer
      - .actual_access:  write_only
        .address_space:  global
        .offset:         120
        .size:           8
        .value_kind:     global_buffer
      - .actual_access:  write_only
        .address_space:  global
        .offset:         128
        .size:           8
        .value_kind:     global_buffer
      - .actual_access:  write_only
        .address_space:  global
        .offset:         136
        .size:           8
        .value_kind:     global_buffer
      - .actual_access:  read_only
        .address_space:  global
        .offset:         144
        .size:           8
        .value_kind:     global_buffer
      - .actual_access:  read_only
        .address_space:  global
        .offset:         152
        .size:           8
        .value_kind:     global_buffer
      - .actual_access:  read_only
        .address_space:  global
        .offset:         160
        .size:           8
        .value_kind:     global_buffer
      - .actual_access:  write_only
        .address_space:  global
        .offset:         168
        .size:           8
        .value_kind:     global_buffer
    .group_segment_fixed_size: 4272
    .kernarg_segment_align: 8
    .kernarg_segment_size: 176
    .language:       OpenCL C
    .language_version:
      - 2
      - 0
    .max_flat_workgroup_size: 256
    .name:           _ZN12_GLOBAL__N_16k_prepEPKfPKiS1_S1_S1_S1_S1_S1_S1_S1_S1_S1_P15HIP_vector_typeIjLj4EEPiPfPDF16_S9_S9_S1_S1_S1_S8_
    .private_segment_fixed_size: 0
    .sgpr_count:     30
    .sgpr_spill_count: 0
    .symbol:         _ZN12_GLOBAL__N_16k_prepEPKfPKiS1_S1_S1_S1_S1_S1_S1_S1_S1_S1_P15HIP_vector_typeIjLj4EEPiPfPDF16_S9_S9_S1_S1_S1_S8_.kd
    .uniform_work_group_size: 1
    .uses_dynamic_stack: false
    .vgpr_count:     144
    .vgpr_spill_count: 0
    .wavefront_size: 64
  - .agpr_count:     0
    .args:
      - .actual_access:  read_only
        .address_space:  global
        .offset:         0
        .size:           8
        .value_kind:     global_buffer
      - .actual_access:  read_only
        .address_space:  global
        .offset:         8
        .size:           8
        .value_kind:     global_buffer
      - .actual_access:  write_only
        .address_space:  global
        .offset:         16
        .size:           8
        .value_kind:     global_buffer
      - .actual_access:  write_only
        .address_space:  global
        .offset:         24
        .size:           8
        .value_kind:     global_buffer
      - .actual_access:  read_only
        .address_space:  global
        .offset:         32
        .size:           8
        .value_kind:     global_buffer
      - .actual_access:  read_only
        .address_space:  global
        .offset:         40
        .size:           8
        .value_kind:     global_buffer
      - .actual_access:  write_only
        .address_space:  global
        .offset:         48
        .size:           8
        .value_kind:     global_buffer
      - .actual_access:  write_only
        .address_space:  global
        .offset:         56
        .size:           8
        .value_kind:     global_buffer
      - .actual_access:  write_only
        .address_space:  global
        .offset:         64
        .size:           8
        .value_kind:     global_buffer
    .group_segment_fixed_size: 7268
    .kernarg_segment_align: 8
    .kernarg_segment_size: 72
    .language:       OpenCL C
    .language_version:
      - 2
      - 0
    .max_flat_workgroup_size: 1024
    .name:           _ZN12_GLOBAL__N_18k_bucketEPK15HIP_vector_typeIjLj4EEPKiPiPS1_PKfS9_PDF16_PfSB_
    .private_segment_fixed_size: 0
    .sgpr_count:     32
    .sgpr_spill_count: 0
    .symbol:         _ZN12_GLOBAL__N_18k_bucketEPK15HIP_vector_typeIjLj4EEPKiPiPS1_PKfS9_PDF16_PfSB_.kd
    .uniform_work_group_size: 1
    .uses_dynamic_stack: false
    .vgpr_count:     62
    .vgpr_spill_count: 0
    .wavefront_size: 64
  - .agpr_count:     0
    .args:
      - .actual_access:  read_only
        .address_space:  global
        .offset:         0
        .size:           8
        .value_kind:     global_buffer
      - .actual_access:  read_only
        .address_space:  global
        .offset:         8
        .size:           8
        .value_kind:     global_buffer
      - .actual_access:  read_only
        .address_space:  global
        .offset:         16
        .size:           8
        .value_kind:     global_buffer
      - .actual_access:  read_only
        .address_space:  global
        .offset:         24
        .size:           8
        .value_kind:     global_buffer
      - .actual_access:  read_only
        .address_space:  global
        .offset:         32
        .size:           8
        .value_kind:     global_buffer
      - .actual_access:  read_only
        .address_space:  global
        .offset:         40
        .size:           8
        .value_kind:     global_buffer
      - .actual_access:  read_only
        .address_space:  global
        .offset:         48
        .size:           8
        .value_kind:     global_buffer
      - .actual_access:  read_only
        .address_space:  global
        .offset:         56
        .size:           8
        .value_kind:     global_buffer
      - .actual_access:  read_only
        .address_space:  global
        .offset:         64
        .size:           8
        .value_kind:     global_buffer
      - .actual_access:  read_only
        .address_space:  global
        .offset:         72
        .size:           8
        .value_kind:     global_buffer
      - .actual_access:  write_only
        .address_space:  global
        .offset:         80
        .size:           8
        .value_kind:     global_buffer
      - .actual_access:  write_only
        .address_space:  global
        .offset:         88
        .size:           8
        .value_kind:     global_buffer
      - .actual_access:  write_only
        .address_space:  global
        .offset:         96
        .size:           8
        .value_kind:     global_buffer
      - .actual_access:  read_only
        .address_space:  global
        .offset:         104
        .size:           8
        .value_kind:     global_buffer
    .group_segment_fixed_size: 25216
    .kernarg_segment_align: 8
    .kernarg_segment_size: 112
    .language:       OpenCL C
    .language_version:
      - 2
      - 0
    .max_flat_workgroup_size: 256
    .name:           _ZN12_GLOBAL__N_18k_layer1EPKDF16_PKfS3_PKiPK15HIP_vector_typeIjLj4EES1_S3_S1_S3_S3_PDF16_PfSB_S3_
    .private_segment_fixed_size: 0
    .sgpr_count:     106
    .sgpr_spill_count: 0
    .symbol:         _ZN12_GLOBAL__N_18k_layer1EPKDF16_PKfS3_PKiPK15HIP_vector_typeIjLj4EES1_S3_S1_S3_S3_PDF16_PfSB_S3_.kd
    .uniform_work_group_size: 1
    .uses_dynamic_stack: false
    .vgpr_count:     96
    .vgpr_spill_count: 0
    .wavefront_size: 64
  - .agpr_count:     0
    .args:
      - .actual_access:  read_only
        .address_space:  global
        .offset:         0
        .size:           8
        .value_kind:     global_buffer
      - .actual_access:  read_only
        .address_space:  global
        .offset:         8
        .size:           8
        .value_kind:     global_buffer
      - .actual_access:  read_only
        .address_space:  global
        .offset:         16
        .size:           8
        .value_kind:     global_buffer
      - .actual_access:  read_only
        .address_space:  global
        .offset:         24
        .size:           8
        .value_kind:     global_buffer
      - .actual_access:  read_only
        .address_space:  global
        .offset:         32
        .size:           8
        .value_kind:     global_buffer
      - .actual_access:  read_only
        .address_space:  global
        .offset:         40
        .size:           8
        .value_kind:     global_buffer
      - .actual_access:  read_only
        .address_space:  global
        .offset:         48
        .size:           8
        .value_kind:     global_buffer
      - .actual_access:  write_only
        .address_space:  global
        .offset:         56
        .size:           8
        .value_kind:     global_buffer
    .group_segment_fixed_size: 6144
    .kernarg_segment_align: 8
    .kernarg_segment_size: 64
    .language:       OpenCL C
    .language_version:
      - 2
      - 0
    .max_flat_workgroup_size: 256
    .name:           _ZN12_GLOBAL__N_18k_layer2EPKDF16_PKfS3_PKiPK15HIP_vector_typeIjLj4EES3_S3_PDF16_
    .private_segment_fixed_size: 0
    .sgpr_count:     42
    .sgpr_spill_count: 0
    .symbol:         _ZN12_GLOBAL__N_18k_layer2EPKDF16_PKfS3_PKiPK15HIP_vector_typeIjLj4EES3_S3_PDF16_.kd
    .uniform_work_group_size: 1
    .uses_dynamic_stack: false
    .vgpr_count:     70
    .vgpr_spill_count: 0
    .wavefront_size: 64
  - .agpr_count:     0
    .args:
      - .actual_access:  read_only
        .address_space:  global
        .offset:         0
        .size:           8
        .value_kind:     global_buffer
      - .actual_access:  read_only
        .address_space:  global
        .offset:         8
        .size:           8
        .value_kind:     global_buffer
      - .actual_access:  read_only
        .address_space:  global
        .offset:         16
        .size:           8
        .value_kind:     global_buffer
      - .actual_access:  read_only
        .address_space:  global
        .offset:         24
        .size:           8
        .value_kind:     global_buffer
      - .actual_access:  read_only
        .address_space:  global
        .offset:         32
        .size:           8
        .value_kind:     global_buffer
      - .actual_access:  read_only
        .address_space:  global
        .offset:         40
        .size:           8
        .value_kind:     global_buffer
      - .actual_access:  write_only
        .address_space:  global
        .offset:         48
        .size:           8
        .value_kind:     global_buffer
    .group_segment_fixed_size: 16384
    .kernarg_segment_align: 8
    .kernarg_segment_size: 56
    .language:       OpenCL C
    .language_version:
      - 2
      - 0
    .max_flat_workgroup_size: 512
    .name:           _ZN12_GLOBAL__N_17k_pairsEPKDF16_PKiS1_PKfS5_S5_Pf
    .private_segment_fixed_size: 0
    .sgpr_count:     18
    .sgpr_spill_count: 0
    .symbol:         _ZN12_GLOBAL__N_17k_pairsEPKDF16_PKiS1_PKfS5_S5_Pf.kd
    .uniform_work_group_size: 1
    .uses_dynamic_stack: false
    .vgpr_count:     59
    .vgpr_spill_count: 0
    .wavefront_size: 64
